# final phase hand-written (all expert-row loads issued before any wait); its residual rows x1 are staged into LDS by LDS-DMA while the last grid barrier is in flight
# speedup vs baseline: 1.0057x; 1.0020x over previous
.LBB0_1188:
	s_waitcnt vmcnt(0)
	s_barrier
	v_readfirstlane_b32 s62, v186
	v_readlane_b32 s64, v235, 0
	v_readlane_b32 s65, v235, 1
	v_readlane_b32 s63, v235, 16
	v_and_b32_e32 v238, 63, v186
	v_lshlrev_b32_e32 v238, 4, v238
	s_lshr_b32 s62, s62, 6
	s_cmp_eq_u32 s62, 0
	s_cbranch_scc1 .Lx1_none
	s_add_u32 s64, s64, 0x9f73000
	s_addc_u32 s65, s65, 0
	s_lshl_b32 s63, s63, 15
	s_add_u32 s64, s64, s63
	s_addc_u32 s65, s65, 0
	s_mov_b32 s67, s62
.Lx1_set:
	s_lshl_b32 s66, s67, 12
	s_add_u32 s68, s64, s66
	s_addc_u32 s69, s65, 0
	s_lshl_b32 s66, s67, 14
	s_add_i32 m0, s66, 0x0
	s_add_u32 s60, s68, 0x0
	s_addc_u32 s61, s69, 0
	global_load_lds_dwordx4 v238, s[60:61]
	s_add_i32 m0, s66, 0x400
	s_add_u32 s60, s68, 0x400
	s_addc_u32 s61, s69, 0
	global_load_lds_dwordx4 v238, s[60:61]
	s_add_i32 m0, s66, 0x800
	s_add_u32 s60, s68, 0x800
	s_addc_u32 s61, s69, 0
	global_load_lds_dwordx4 v238, s[60:61]
	s_add_i32 m0, s66, 0xc00
	s_add_u32 s60, s68, 0xc00
	s_addc_u32 s61, s69, 0
	global_load_lds_dwordx4 v238, s[60:61]
	s_add_i32 m0, s66, 0x1000
	s_add_u32 s60, s68, 0x800000
	s_addc_u32 s61, s69, 0
	global_load_lds_dwordx4 v238, s[60:61]
	s_add_i32 m0, s66, 0x1400
	s_add_u32 s60, s68, 0x800400
	s_addc_u32 s61, s69, 0
	global_load_lds_dwordx4 v238, s[60:61]
	s_add_i32 m0, s66, 0x1800
	s_add_u32 s60, s68, 0x800800
	s_addc_u32 s61, s69, 0
	global_load_lds_dwordx4 v238, s[60:61]
	s_add_i32 m0, s66, 0x1c00
	s_add_u32 s60, s68, 0x800c00
	s_addc_u32 s61, s69, 0
	global_load_lds_dwordx4 v238, s[60:61]
	s_add_i32 m0, s66, 0x2000
	s_add_u32 s60, s68, 0x1000000
	s_addc_u32 s61, s69, 0
	global_load_lds_dwordx4 v238, s[60:61]
	s_add_i32 m0, s66, 0x2400
	s_add_u32 s60, s68, 0x1000400
	s_addc_u32 s61, s69, 0
	global_load_lds_dwordx4 v238, s[60:61]
	s_add_i32 m0, s66, 0x2800
	s_add_u32 s60, s68, 0x1000800
	s_addc_u32 s61, s69, 0
	global_load_lds_dwordx4 v238, s[60:61]
	s_add_i32 m0, s66, 0x2c00
	s_add_u32 s60, s68, 0x1000c00
	s_addc_u32 s61, s69, 0
	global_load_lds_dwordx4 v238, s[60:61]
	s_add_i32 m0, s66, 0x3000
	s_add_u32 s60, s68, 0x1800000
	s_addc_u32 s61, s69, 0
	global_load_lds_dwordx4 v238, s[60:61]
	s_add_i32 m0, s66, 0x3400
	s_add_u32 s60, s68, 0x1800400
	s_addc_u32 s61, s69, 0
	global_load_lds_dwordx4 v238, s[60:61]
	s_add_i32 m0, s66, 0x3800
	s_add_u32 s60, s68, 0x1800800
	s_addc_u32 s61, s69, 0
	global_load_lds_dwordx4 v238, s[60:61]
	s_add_i32 m0, s66, 0x3c00
	s_add_u32 s60, s68, 0x1800c00
	s_addc_u32 s61, s69, 0
	global_load_lds_dwordx4 v238, s[60:61]
	s_cmp_eq_u32 s67, 1
	s_cbranch_scc0 .Lx1_none
	s_mov_b32 s67, 0
	s_branch .Lx1_set
.Lx1_none:
	s_mov_b64 s[0:1], exec
	v_readlane_b32 s2, v235, 5
	v_readlane_b32 s3, v235, 6
	s_and_b64 s[2:3], s[0:1], s[2:3]
	v_readlane_b32 s46, v235, 14
	s_xor_b64 s[0:1], s[2:3], s[0:1]
	v_readlane_b32 s47, v235, 15
	s_mov_b64 exec, s[2:3]
	s_cbranch_execz .LBB0_1241
	s_cmp_eq_u32 s98, 0
	s_cbranch_scc1 .Lxb_nopend_11
	v_readlane_b32 s100, v235, 7
	v_readlane_b32 s101, v235, 8
	v_mov_b32_e32 v237, 0x3400
	s_nop 3

.LBB0_1241:
	s_or_b64 exec, exec, s[0:1]
	s_waitcnt lgkmcnt(0)
	s_waitcnt vmcnt(0)
	s_barrier
	v_readlane_b32 s6, v235, 16
	v_readlane_b32 s7, v235, 2
	v_and_b32_e32 v0, 63, v186
	v_lshrrev_b32_e32 v11, 6, v186
	s_load_dwordx2 s[4:5], s[46:47], 0x98
	s_load_dwordx4 s[0:3], s[46:47], 0x88
	v_readfirstlane_b32 s8, v11
	v_lshlrev_b32_e32 v1, 4, v0
	v_lshlrev_b32_e32 v11, 14, v11
	v_add_u32_e32 v11, v11, v1
	v_lshlrev_b32_e32 v2, 5, v0
	v_and_b32_e32 v3, 31, v0
	v_lshlrev_b32_e32 v3, 2, v3
	v_xor_b32_e32 v4, 32, v0
	v_lshlrev_b32_e32 v4, 2, v4
	v_xor_b32_e32 v5, 16, v0
	v_lshlrev_b32_e32 v5, 2, v5
	v_xor_b32_e32 v6, 8, v0
	v_lshlrev_b32_e32 v6, 2, v6
	v_xor_b32_e32 v7, 4, v0
	v_lshlrev_b32_e32 v7, 2, v7
	v_xor_b32_e32 v8, 2, v0
	v_lshlrev_b32_e32 v8, 2, v8
	v_xor_b32_e32 v9, 1, v0
	v_lshlrev_b32_e32 v9, 2, v9
	v_mov_b32_e32 v10, 0x358637bd
	s_lshl_b32 s6, s6, 4
	s_lshl_b32 s8, s8, 1
	s_add_i32 s6, s6, s8
	s_lshl_b32 s7, s7, 4
	s_mov_b32 s23, 0x3a800000
	s_cmp_lt_u32 s6, 0x4000
	s_cbranch_scc0 .Lfin_end
	s_waitcnt lgkmcnt(0)
	s_add_u32 s14, s4, 0x1b73000
	s_addc_u32 s15, s5, 0
	s_add_u32 s16, s4, 0x9f73000
	s_addc_u32 s17, s5, 0
	s_add_u32 s18, s4, 0x15b000
	s_addc_u32 s19, s5, 0
	s_add_u32 s20, s4, 0x5000
	s_addc_u32 s21, s5, 0
	s_add_u32 s34, s20, 0x6000
	s_addc_u32 s35, s21, 0
	global_load_dwordx4 v[12:15], v2, s[0:1]
	global_load_dwordx4 v[16:19], v2, s[0:1] offset:16
	global_load_dwordx4 v[20:23], v2, s[0:1] offset:2048
	global_load_dwordx4 v[24:27], v2, s[0:1] offset:2064
	global_load_dwordx4 v[28:31], v2, s[20:21]
	global_load_dwordx4 v[32:35], v2, s[20:21] offset:16
	global_load_dwordx4 v[36:39], v2, s[20:21] offset:2048
	global_load_dwordx4 v[40:43], v2, s[20:21] offset:2064
	global_load_dwordx4 v[44:47], v2, s[34:35]
	global_load_dwordx4 v[48:51], v2, s[34:35] offset:16
	global_load_dwordx4 v[52:55], v2, s[34:35] offset:2048
	global_load_dwordx4 v[56:59], v2, s[34:35] offset:2064
	s_lshl_b32 s26, s6, 6
	s_add_u32 s24, s18, s26
	s_addc_u32 s25, s19, 0
	global_load_dword v77, v3, s[24:25]
	s_waitcnt vmcnt(0)
	s_branch .Lfin_body
.Lfin_loop:
	s_waitcnt vmcnt(8)
.Lfin_body:
	ds_read_b128 v[80:83], v11
	ds_read_b128 v[84:87], v11 offset:1024
	ds_read_b128 v[88:91], v11 offset:2048
	ds_read_b128 v[92:95], v11 offset:3072
	v_add_u32_e32 v11, 0x1000, v11
	s_waitcnt lgkmcnt(0)
	v_mov_b32_e32 v76, v77
	v_cvt_f32_f16_e32 v96, v80
	v_cvt_f32_f16_sdwa v97, v80 dst_sel:DWORD dst_unused:UNUSED_PAD src0_sel:WORD_1
	v_cvt_f32_f16_e32 v98, v81
	v_cvt_f32_f16_sdwa v99, v81 dst_sel:DWORD dst_unused:UNUSED_PAD src0_sel:WORD_1
	v_cvt_f32_f16_e32 v100, v82
	v_cvt_f32_f16_sdwa v101, v82 dst_sel:DWORD dst_unused:UNUSED_PAD src0_sel:WORD_1
	v_cvt_f32_f16_e32 v102, v83
	v_cvt_f32_f16_sdwa v103, v83 dst_sel:DWORD dst_unused:UNUSED_PAD src0_sel:WORD_1
	v_cvt_f32_f16_e32 v104, v84
	v_cvt_f32_f16_sdwa v105, v84 dst_sel:DWORD dst_unused:UNUSED_PAD src0_sel:WORD_1
	v_cvt_f32_f16_e32 v106, v85
	v_cvt_f32_f16_sdwa v107, v85 dst_sel:DWORD dst_unused:UNUSED_PAD src0_sel:WORD_1
	v_cvt_f32_f16_e32 v108, v86
	v_cvt_f32_f16_sdwa v109, v86 dst_sel:DWORD dst_unused:UNUSED_PAD src0_sel:WORD_1
	v_cvt_f32_f16_e32 v110, v87
	v_cvt_f32_f16_sdwa v111, v87 dst_sel:DWORD dst_unused:UNUSED_PAD src0_sel:WORD_1
	v_cvt_f32_f16_e32 v112, v88
	v_cvt_f32_f16_sdwa v113, v88 dst_sel:DWORD dst_unused:UNUSED_PAD src0_sel:WORD_1
	v_cvt_f32_f16_e32 v114, v89
	v_cvt_f32_f16_sdwa v115, v89 dst_sel:DWORD dst_unused:UNUSED_PAD src0_sel:WORD_1
	v_cvt_f32_f16_e32 v116, v90
	v_cvt_f32_f16_sdwa v117, v90 dst_sel:DWORD dst_unused:UNUSED_PAD src0_sel:WORD_1
	v_cvt_f32_f16_e32 v118, v91
	v_cvt_f32_f16_sdwa v119, v91 dst_sel:DWORD dst_unused:UNUSED_PAD src0_sel:WORD_1
	v_cvt_f32_f16_e32 v120, v92
	v_cvt_f32_f16_sdwa v121, v92 dst_sel:DWORD dst_unused:UNUSED_PAD src0_sel:WORD_1
	v_cvt_f32_f16_e32 v122, v93
	v_cvt_f32_f16_sdwa v123, v93 dst_sel:DWORD dst_unused:UNUSED_PAD src0_sel:WORD_1
	v_cvt_f32_f16_e32 v124, v94
	v_cvt_f32_f16_sdwa v125, v94 dst_sel:DWORD dst_unused:UNUSED_PAD src0_sel:WORD_1
	v_cvt_f32_f16_e32 v126, v95
	v_cvt_f32_f16_sdwa v127, v95 dst_sel:DWORD dst_unused:UNUSED_PAD src0_sel:WORD_1
	v_cmp_lt_i32_e32 vcc, -1, v76
	v_mov_b32_e32 v128, 0
	v_mov_b32_e32 v129, 0
	v_mov_b32_e32 v130, 0
	v_mov_b32_e32 v131, 0
	v_mov_b32_e32 v132, 0
	v_mov_b32_e32 v133, 0
	v_mov_b32_e32 v134, 0
	v_mov_b32_e32 v135, 0
	v_mov_b32_e32 v136, 0
	v_mov_b32_e32 v137, 0
	v_mov_b32_e32 v138, 0
	v_mov_b32_e32 v139, 0
	v_mov_b32_e32 v140, 0
	v_mov_b32_e32 v141, 0
	v_mov_b32_e32 v142, 0
	v_mov_b32_e32 v143, 0
	v_mov_b32_e32 v144, 0
	v_mov_b32_e32 v145, 0
	v_mov_b32_e32 v146, 0
	v_mov_b32_e32 v147, 0
	v_mov_b32_e32 v148, 0
	v_mov_b32_e32 v149, 0
	v_mov_b32_e32 v150, 0
	v_mov_b32_e32 v151, 0
	v_mov_b32_e32 v152, 0
	v_mov_b32_e32 v153, 0
	v_mov_b32_e32 v154, 0
	v_mov_b32_e32 v155, 0
	v_mov_b32_e32 v156, 0
	v_mov_b32_e32 v157, 0
	v_mov_b32_e32 v158, 0
	v_mov_b32_e32 v159, 0
	s_and_b32 s9, vcc_lo, 0xffff
	s_lshr_b32 s10, vcc_lo, 16
	s_and_b32 s10, s10, 0xffff
	s_bcnt1_i32_b32 s11, s9
	s_bcnt1_i32_b32 s12, s10
	s_lshr_b32 s22, s6, 13
	s_lshl_b32 s22, s22, 10
	s_cmp_eq_u32 s22, 0
	s_cbranch_scc0 .Lfin_gt1
	v_mov_b32_e32 v60, v28
	v_mov_b32_e32 v61, v29
	v_mov_b32_e32 v62, v30
	v_mov_b32_e32 v63, v31
	v_mov_b32_e32 v64, v32
	v_mov_b32_e32 v65, v33
	v_mov_b32_e32 v66, v34
	v_mov_b32_e32 v67, v35
	v_mov_b32_e32 v68, v36
	v_mov_b32_e32 v69, v37
	v_mov_b32_e32 v70, v38
	v_mov_b32_e32 v71, v39
	v_mov_b32_e32 v72, v40
	v_mov_b32_e32 v73, v41
	v_mov_b32_e32 v74, v42
	v_mov_b32_e32 v75, v43
	s_branch .Lfin_gtd
.Lfin_gt1:
	v_mov_b32_e32 v60, v44
	v_mov_b32_e32 v61, v45
	v_mov_b32_e32 v62, v46
	v_mov_b32_e32 v63, v47
	v_mov_b32_e32 v64, v48
	v_mov_b32_e32 v65, v49
	v_mov_b32_e32 v66, v50
	v_mov_b32_e32 v67, v51
	v_mov_b32_e32 v68, v52
	v_mov_b32_e32 v69, v53
	v_mov_b32_e32 v70, v54
	v_mov_b32_e32 v71, v55
	v_mov_b32_e32 v72, v56
	v_mov_b32_e32 v73, v57
	v_mov_b32_e32 v74, v58
	v_mov_b32_e32 v75, v59
.Lfin_gtd:
	s_cmp_eq_u32 s9, 0
	s_cbranch_scc1 .Lfin_iss0
	s_ff1_i32_b32 s26, s9
	s_bitset0_b32 s9, s26
	v_readlane_b32 s30, v76, s26
	s_lshl_b32 s26, s26, 11
	s_add_i32 s26, s26, s22
	s_add_i32 s26, s26, s30
	s_lshl_b32 s26, s26, 11
	s_add_u32 s24, s14, s26
	s_addc_u32 s25, s15, 0
	global_load_dwordx4 v[160:163], v1, s[24:25]
	global_load_dwordx4 v[164:167], v1, s[24:25] offset:1024
	s_cmp_eq_u32 s9, 0
	s_cbranch_scc1 .Lfin_iss0
	s_ff1_i32_b32 s26, s9
	s_bitset0_b32 s9, s26
	v_readlane_b32 s30, v76, s26
	s_lshl_b32 s26, s26, 11
	s_add_i32 s26, s26, s22
	s_add_i32 s26, s26, s30
	s_lshl_b32 s26, s26, 11
	s_add_u32 s24, s14, s26
	s_addc_u32 s25, s15, 0
	global_load_dwordx4 v[168:171], v1, s[24:25]
	global_load_dwordx4 v[172:175], v1, s[24:25] offset:1024
	s_cmp_eq_u32 s9, 0
	s_cbranch_scc1 .Lfin_iss0
	s_ff1_i32_b32 s26, s9
	s_bitset0_b32 s9, s26
	v_readlane_b32 s30, v76, s26
	s_lshl_b32 s26, s26, 11
	s_add_i32 s26, s26, s22
	s_add_i32 s26, s26, s30
	s_lshl_b32 s26, s26, 11
	s_add_u32 s24, s14, s26
	s_addc_u32 s25, s15, 0
	global_load_dwordx4 v[176:179], v1, s[24:25]
	global_load_dwordx4 v[180:183], v1, s[24:25] offset:1024
	s_cmp_eq_u32 s9, 0
	s_cbranch_scc1 .Lfin_iss0
	s_ff1_i32_b32 s26, s9
	s_bitset0_b32 s9, s26
	v_readlane_b32 s30, v76, s26
	s_lshl_b32 s26, s26, 11
	s_add_i32 s26, s26, s22
	s_add_i32 s26, s26, s30
	s_lshl_b32 s26, s26, 11
	s_add_u32 s24, s14, s26
	s_addc_u32 s25, s15, 0
	global_load_dwordx4 v[184:187], v1, s[24:25]
	global_load_dwordx4 v[188:191], v1, s[24:25] offset:1024
	s_cmp_eq_u32 s9, 0
	s_cbranch_scc1 .Lfin_iss0
	s_ff1_i32_b32 s26, s9
	s_bitset0_b32 s9, s26
	v_readlane_b32 s30, v76, s26
	s_lshl_b32 s26, s26, 11
	s_add_i32 s26, s26, s22
	s_add_i32 s26, s26, s30
	s_lshl_b32 s26, s26, 11
	s_add_u32 s24, s14, s26
	s_addc_u32 s25, s15, 0
	global_load_dwordx4 v[192:195], v1, s[24:25]
	global_load_dwordx4 v[196:199], v1, s[24:25] offset:1024
	s_cmp_eq_u32 s9, 0
	s_cbranch_scc1 .Lfin_iss0
	s_ff1_i32_b32 s26, s9
	s_bitset0_b32 s9, s26
	v_readlane_b32 s30, v76, s26
	s_lshl_b32 s26, s26, 11
	s_add_i32 s26, s26, s22
	s_add_i32 s26, s26, s30
	s_lshl_b32 s26, s26, 11
	s_add_u32 s24, s14, s26
	s_addc_u32 s25, s15, 0
	global_load_dwordx4 v[200:203], v1, s[24:25]
	global_load_dwordx4 v[204:207], v1, s[24:25] offset:1024
.Lfin_iss0:
	s_cmp_eq_u32 s10, 0
	s_cbranch_scc1 .Lfin_iss1
	s_ff1_i32_b32 s26, s10
	s_bitset0_b32 s10, s26
	s_add_i32 s27, s26, 16
	v_readlane_b32 s30, v76, s27
	s_lshl_b32 s26, s26, 11
	s_add_i32 s26, s26, s22
	s_add_i32 s26, s26, s30
	s_lshl_b32 s26, s26, 11
	s_add_u32 s24, s14, s26
	s_addc_u32 s25, s15, 0
	global_load_dwordx4 v[208:211], v1, s[24:25]
	global_load_dwordx4 v[212:215], v1, s[24:25] offset:1024
	s_cmp_eq_u32 s10, 0
	s_cbranch_scc1 .Lfin_iss1
	s_ff1_i32_b32 s26, s10
	s_bitset0_b32 s10, s26
	s_add_i32 s27, s26, 16
	v_readlane_b32 s30, v76, s27
	s_lshl_b32 s26, s26, 11
	s_add_i32 s26, s26, s22
	s_add_i32 s26, s26, s30
	s_lshl_b32 s26, s26, 11
	s_add_u32 s24, s14, s26
	s_addc_u32 s25, s15, 0
	global_load_dwordx4 v[216:219], v1, s[24:25]
	global_load_dwordx4 v[220:223], v1, s[24:25] offset:1024
	s_cmp_eq_u32 s10, 0
	s_cbranch_scc1 .Lfin_iss1
	s_ff1_i32_b32 s26, s10
	s_bitset0_b32 s10, s26
	s_add_i32 s27, s26, 16
	v_readlane_b32 s30, v76, s27
	s_lshl_b32 s26, s26, 11
	s_add_i32 s26, s26, s22
	s_add_i32 s26, s26, s30
	s_lshl_b32 s26, s26, 11
	s_add_u32 s24, s14, s26
	s_addc_u32 s25, s15, 0
	global_load_dwordx4 v[224:227], v1, s[24:25]
	global_load_dwordx4 v[228:231], v1, s[24:25] offset:1024
	s_cmp_eq_u32 s10, 0
	s_cbranch_scc1 .Lfin_iss1
	s_ff1_i32_b32 s26, s10
	s_bitset0_b32 s10, s26
	s_add_i32 s27, s26, 16
	v_readlane_b32 s30, v76, s27
	s_lshl_b32 s26, s26, 11
	s_add_i32 s26, s26, s22
	s_add_i32 s26, s26, s30
	s_lshl_b32 s26, s26, 11
	s_add_u32 s24, s14, s26
	s_addc_u32 s25, s15, 0
	global_load_dwordx4 v[232:235], v1, s[24:25]
	global_load_dwordx4 v[236:239], v1, s[24:25] offset:1024
	s_cmp_eq_u32 s10, 0
	s_cbranch_scc1 .Lfin_iss1
	s_ff1_i32_b32 s26, s10
	s_bitset0_b32 s10, s26
	s_add_i32 s27, s26, 16
	v_readlane_b32 s30, v76, s27
	s_lshl_b32 s26, s26, 11
	s_add_i32 s26, s26, s22
	s_add_i32 s26, s26, s30
	s_lshl_b32 s26, s26, 11
	s_add_u32 s24, s14, s26
	s_addc_u32 s25, s15, 0
	global_load_dwordx4 v[240:243], v1, s[24:25]
	global_load_dwordx4 v[244:247], v1, s[24:25] offset:1024
	s_cmp_eq_u32 s10, 0
	s_cbranch_scc1 .Lfin_iss1
	s_ff1_i32_b32 s26, s10
	s_bitset0_b32 s10, s26
	s_add_i32 s27, s26, 16
	v_readlane_b32 s30, v76, s27
	s_lshl_b32 s26, s26, 11
	s_add_i32 s26, s26, s22
	s_add_i32 s26, s26, s30
	s_lshl_b32 s26, s26, 11
	s_add_u32 s24, s14, s26
	s_addc_u32 s25, s15, 0
	global_load_dwordx4 v[248:251], v1, s[24:25]
	global_load_dwordx4 v[252:255], v1, s[24:25] offset:1024
.Lfin_iss1:
	s_add_i32 s8, s6, s7
	s_cmp_lt_u32 s8, 0x4000
	s_cbranch_scc0 .Lfin_nopf
	s_lshl_b32 s26, s8, 6
	s_add_u32 s24, s18, s26
	s_addc_u32 s25, s19, 0
	global_load_dword v77, v3, s[24:25]
	s_waitcnt vmcnt(1)
	s_branch .Lfin_acc

.Lfin_acc:
	s_cmp_lt_u32 s11, 1
	s_cbranch_scc1 .Lfin_accd0
	v_lshlrev_b32_e32 v78, 16, v160
	v_and_b32_e32 v79, 0xffff0000, v160
	v_pk_add_f32 v[128:129], v[128:129], v[78:79]
	v_lshlrev_b32_e32 v78, 16, v161
	v_and_b32_e32 v79, 0xffff0000, v161
	v_pk_add_f32 v[130:131], v[130:131], v[78:79]
	v_lshlrev_b32_e32 v78, 16, v162
	v_and_b32_e32 v79, 0xffff0000, v162
	v_pk_add_f32 v[132:133], v[132:133], v[78:79]
	v_lshlrev_b32_e32 v78, 16, v163
	v_and_b32_e32 v79, 0xffff0000, v163
	v_pk_add_f32 v[134:135], v[134:135], v[78:79]
	v_lshlrev_b32_e32 v78, 16, v164
	v_and_b32_e32 v79, 0xffff0000, v164
	v_pk_add_f32 v[136:137], v[136:137], v[78:79]
	v_lshlrev_b32_e32 v78, 16, v165
	v_and_b32_e32 v79, 0xffff0000, v165
	v_pk_add_f32 v[138:139], v[138:139], v[78:79]
	v_lshlrev_b32_e32 v78, 16, v166
	v_and_b32_e32 v79, 0xffff0000, v166
	v_pk_add_f32 v[140:141], v[140:141], v[78:79]
	v_lshlrev_b32_e32 v78, 16, v167
	v_and_b32_e32 v79, 0xffff0000, v167
	v_pk_add_f32 v[142:143], v[142:143], v[78:79]
	s_cmp_lt_u32 s11, 2
	s_cbranch_scc1 .Lfin_accd0
	v_lshlrev_b32_e32 v78, 16, v168
	v_and_b32_e32 v79, 0xffff0000, v168
	v_pk_add_f32 v[128:129], v[128:129], v[78:79]
	v_lshlrev_b32_e32 v78, 16, v169
	v_and_b32_e32 v79, 0xffff0000, v169
	v_pk_add_f32 v[130:131], v[130:131], v[78:79]
	v_lshlrev_b32_e32 v78, 16, v170
	v_and_b32_e32 v79, 0xffff0000, v170
	v_pk_add_f32 v[132:133], v[132:133], v[78:79]
	v_lshlrev_b32_e32 v78, 16, v171
	v_and_b32_e32 v79, 0xffff0000, v171
	v_pk_add_f32 v[134:135], v[134:135], v[78:79]
	v_lshlrev_b32_e32 v78, 16, v172
	v_and_b32_e32 v79, 0xffff0000, v172
	v_pk_add_f32 v[136:137], v[136:137], v[78:79]
	v_lshlrev_b32_e32 v78, 16, v173
	v_and_b32_e32 v79, 0xffff0000, v173
	v_pk_add_f32 v[138:139], v[138:139], v[78:79]
	v_lshlrev_b32_e32 v78, 16, v174
	v_and_b32_e32 v79, 0xffff0000, v174
	v_pk_add_f32 v[140:141], v[140:141], v[78:79]
	v_lshlrev_b32_e32 v78, 16, v175
	v_and_b32_e32 v79, 0xffff0000, v175
	v_pk_add_f32 v[142:143], v[142:143], v[78:79]
	s_cmp_lt_u32 s11, 3
	s_cbranch_scc1 .Lfin_accd0
	v_lshlrev_b32_e32 v78, 16, v176
	v_and_b32_e32 v79, 0xffff0000, v176
	v_pk_add_f32 v[128:129], v[128:129], v[78:79]
	v_lshlrev_b32_e32 v78, 16, v177
	v_and_b32_e32 v79, 0xffff0000, v177
	v_pk_add_f32 v[130:131], v[130:131], v[78:79]
	v_lshlrev_b32_e32 v78, 16, v178
	v_and_b32_e32 v79, 0xffff0000, v178
	v_pk_add_f32 v[132:133], v[132:133], v[78:79]
	v_lshlrev_b32_e32 v78, 16, v179
	v_and_b32_e32 v79, 0xffff0000, v179
	v_pk_add_f32 v[134:135], v[134:135], v[78:79]
	v_lshlrev_b32_e32 v78, 16, v180
	v_and_b32_e32 v79, 0xffff0000, v180
	v_pk_add_f32 v[136:137], v[136:137], v[78:79]
	v_lshlrev_b32_e32 v78, 16, v181
	v_and_b32_e32 v79, 0xffff0000, v181
	v_pk_add_f32 v[138:139], v[138:139], v[78:79]
	v_lshlrev_b32_e32 v78, 16, v182
	v_and_b32_e32 v79, 0xffff0000, v182
	v_pk_add_f32 v[140:141], v[140:141], v[78:79]
	v_lshlrev_b32_e32 v78, 16, v183
	v_and_b32_e32 v79, 0xffff0000, v183
	v_pk_add_f32 v[142:143], v[142:143], v[78:79]
	s_cmp_lt_u32 s11, 4
	s_cbranch_scc1 .Lfin_accd0
	v_lshlrev_b32_e32 v78, 16, v184
	v_and_b32_e32 v79, 0xffff0000, v184
	v_pk_add_f32 v[128:129], v[128:129], v[78:79]
	v_lshlrev_b32_e32 v78, 16, v185
	v_and_b32_e32 v79, 0xffff0000, v185
	v_pk_add_f32 v[130:131], v[130:131], v[78:79]
	v_lshlrev_b32_e32 v78, 16, v186
	v_and_b32_e32 v79, 0xffff0000, v186
	v_pk_add_f32 v[132:133], v[132:133], v[78:79]
	v_lshlrev_b32_e32 v78, 16, v187
	v_and_b32_e32 v79, 0xffff0000, v187
	v_pk_add_f32 v[134:135], v[134:135], v[78:79]
	v_lshlrev_b32_e32 v78, 16, v188
	v_and_b32_e32 v79, 0xffff0000, v188
	v_pk_add_f32 v[136:137], v[136:137], v[78:79]
	v_lshlrev_b32_e32 v78, 16, v189
	v_and_b32_e32 v79, 0xffff0000, v189
	v_pk_add_f32 v[138:139], v[138:139], v[78:79]
	v_lshlrev_b32_e32 v78, 16, v190
	v_and_b32_e32 v79, 0xffff0000, v190
	v_pk_add_f32 v[140:141], v[140:141], v[78:79]
	v_lshlrev_b32_e32 v78, 16, v191
	v_and_b32_e32 v79, 0xffff0000, v191
	v_pk_add_f32 v[142:143], v[142:143], v[78:79]
	s_cmp_lt_u32 s11, 5
	s_cbranch_scc1 .Lfin_accd0
	v_lshlrev_b32_e32 v78, 16, v192
	v_and_b32_e32 v79, 0xffff0000, v192
	v_pk_add_f32 v[128:129], v[128:129], v[78:79]
	v_lshlrev_b32_e32 v78, 16, v193
	v_and_b32_e32 v79, 0xffff0000, v193
	v_pk_add_f32 v[130:131], v[130:131], v[78:79]
	v_lshlrev_b32_e32 v78, 16, v194
	v_and_b32_e32 v79, 0xffff0000, v194
	v_pk_add_f32 v[132:133], v[132:133], v[78:79]
	v_lshlrev_b32_e32 v78, 16, v195
	v_and_b32_e32 v79, 0xffff0000, v195
	v_pk_add_f32 v[134:135], v[134:135], v[78:79]
	v_lshlrev_b32_e32 v78, 16, v196
	v_and_b32_e32 v79, 0xffff0000, v196
	v_pk_add_f32 v[136:137], v[136:137], v[78:79]
	v_lshlrev_b32_e32 v78, 16, v197
	v_and_b32_e32 v79, 0xffff0000, v197
	v_pk_add_f32 v[138:139], v[138:139], v[78:79]
	v_lshlrev_b32_e32 v78, 16, v198
	v_and_b32_e32 v79, 0xffff0000, v198
	v_pk_add_f32 v[140:141], v[140:141], v[78:79]
	v_lshlrev_b32_e32 v78, 16, v199
	v_and_b32_e32 v79, 0xffff0000, v199
	v_pk_add_f32 v[142:143], v[142:143], v[78:79]
	s_cmp_lt_u32 s11, 6
	s_cbranch_scc1 .Lfin_accd0
	v_lshlrev_b32_e32 v78, 16, v200
	v_and_b32_e32 v79, 0xffff0000, v200
	v_pk_add_f32 v[128:129], v[128:129], v[78:79]
	v_lshlrev_b32_e32 v78, 16, v201
	v_and_b32_e32 v79, 0xffff0000, v201
	v_pk_add_f32 v[130:131], v[130:131], v[78:79]
	v_lshlrev_b32_e32 v78, 16, v202
	v_and_b32_e32 v79, 0xffff0000, v202
	v_pk_add_f32 v[132:133], v[132:133], v[78:79]
	v_lshlrev_b32_e32 v78, 16, v203
	v_and_b32_e32 v79, 0xffff0000, v203
	v_pk_add_f32 v[134:135], v[134:135], v[78:79]
	v_lshlrev_b32_e32 v78, 16, v204
	v_and_b32_e32 v79, 0xffff0000, v204
	v_pk_add_f32 v[136:137], v[136:137], v[78:79]
	v_lshlrev_b32_e32 v78, 16, v205
	v_and_b32_e32 v79, 0xffff0000, v205
	v_pk_add_f32 v[138:139], v[138:139], v[78:79]
	v_lshlrev_b32_e32 v78, 16, v206
	v_and_b32_e32 v79, 0xffff0000, v206
	v_pk_add_f32 v[140:141], v[140:141], v[78:79]
	v_lshlrev_b32_e32 v78, 16, v207
	v_and_b32_e32 v79, 0xffff0000, v207
	v_pk_add_f32 v[142:143], v[142:143], v[78:79]
.Lfin_ovf0:
	s_cmp_eq_u32 s9, 0
	s_cbranch_scc1 .Lfin_accd0
	s_ff1_i32_b32 s26, s9
	s_bitset0_b32 s9, s26
	v_readlane_b32 s30, v76, s26
	s_lshl_b32 s26, s26, 11
	s_add_i32 s26, s26, s22
	s_add_i32 s26, s26, s30
	s_lshl_b32 s26, s26, 11
	s_add_u32 s24, s14, s26
	s_addc_u32 s25, s15, 0
	global_load_dwordx4 v[160:163], v1, s[24:25]
	global_load_dwordx4 v[164:167], v1, s[24:25] offset:1024
	s_waitcnt vmcnt(0)
	v_lshlrev_b32_e32 v78, 16, v160
	v_and_b32_e32 v79, 0xffff0000, v160
	v_pk_add_f32 v[128:129], v[128:129], v[78:79]
	v_lshlrev_b32_e32 v78, 16, v161
	v_and_b32_e32 v79, 0xffff0000, v161
	v_pk_add_f32 v[130:131], v[130:131], v[78:79]
	v_lshlrev_b32_e32 v78, 16, v162
	v_and_b32_e32 v79, 0xffff0000, v162
	v_pk_add_f32 v[132:133], v[132:133], v[78:79]
	v_lshlrev_b32_e32 v78, 16, v163
	v_and_b32_e32 v79, 0xffff0000, v163
	v_pk_add_f32 v[134:135], v[134:135], v[78:79]
	v_lshlrev_b32_e32 v78, 16, v164
	v_and_b32_e32 v79, 0xffff0000, v164
	v_pk_add_f32 v[136:137], v[136:137], v[78:79]
	v_lshlrev_b32_e32 v78, 16, v165
	v_and_b32_e32 v79, 0xffff0000, v165
	v_pk_add_f32 v[138:139], v[138:139], v[78:79]
	v_lshlrev_b32_e32 v78, 16, v166
	v_and_b32_e32 v79, 0xffff0000, v166
	v_pk_add_f32 v[140:141], v[140:141], v[78:79]
	v_lshlrev_b32_e32 v78, 16, v167
	v_and_b32_e32 v79, 0xffff0000, v167
	v_pk_add_f32 v[142:143], v[142:143], v[78:79]
	s_branch .Lfin_ovf0
.Lfin_accd0:
	s_cmp_lt_u32 s12, 1
	s_cbranch_scc1 .Lfin_accd1
	v_lshlrev_b32_e32 v78, 16, v208
	v_and_b32_e32 v79, 0xffff0000, v208
	v_pk_add_f32 v[144:145], v[144:145], v[78:79]
	v_lshlrev_b32_e32 v78, 16, v209
	v_and_b32_e32 v79, 0xffff0000, v209
	v_pk_add_f32 v[146:147], v[146:147], v[78:79]
	v_lshlrev_b32_e32 v78, 16, v210
	v_and_b32_e32 v79, 0xffff0000, v210
	v_pk_add_f32 v[148:149], v[148:149], v[78:79]
	v_lshlrev_b32_e32 v78, 16, v211
	v_and_b32_e32 v79, 0xffff0000, v211
	v_pk_add_f32 v[150:151], v[150:151], v[78:79]
	v_lshlrev_b32_e32 v78, 16, v212
	v_and_b32_e32 v79, 0xffff0000, v212
	v_pk_add_f32 v[152:153], v[152:153], v[78:79]
	v_lshlrev_b32_e32 v78, 16, v213
	v_and_b32_e32 v79, 0xffff0000, v213
	v_pk_add_f32 v[154:155], v[154:155], v[78:79]
	v_lshlrev_b32_e32 v78, 16, v214
	v_and_b32_e32 v79, 0xffff0000, v214
	v_pk_add_f32 v[156:157], v[156:157], v[78:79]
	v_lshlrev_b32_e32 v78, 16, v215
	v_and_b32_e32 v79, 0xffff0000, v215
	v_pk_add_f32 v[158:159], v[158:159], v[78:79]
	s_cmp_lt_u32 s12, 2
	s_cbranch_scc1 .Lfin_accd1
	v_lshlrev_b32_e32 v78, 16, v216
	v_and_b32_e32 v79, 0xffff0000, v216
	v_pk_add_f32 v[144:145], v[144:145], v[78:79]
	v_lshlrev_b32_e32 v78, 16, v217
	v_and_b32_e32 v79, 0xffff0000, v217
	v_pk_add_f32 v[146:147], v[146:147], v[78:79]
	v_lshlrev_b32_e32 v78, 16, v218
	v_and_b32_e32 v79, 0xffff0000, v218
	v_pk_add_f32 v[148:149], v[148:149], v[78:79]
	v_lshlrev_b32_e32 v78, 16, v219
	v_and_b32_e32 v79, 0xffff0000, v219
	v_pk_add_f32 v[150:151], v[150:151], v[78:79]
	v_lshlrev_b32_e32 v78, 16, v220
	v_and_b32_e32 v79, 0xffff0000, v220
	v_pk_add_f32 v[152:153], v[152:153], v[78:79]
	v_lshlrev_b32_e32 v78, 16, v221
	v_and_b32_e32 v79, 0xffff0000, v221
	v_pk_add_f32 v[154:155], v[154:155], v[78:79]
	v_lshlrev_b32_e32 v78, 16, v222
	v_and_b32_e32 v79, 0xffff0000, v222
	v_pk_add_f32 v[156:157], v[156:157], v[78:79]
	v_lshlrev_b32_e32 v78, 16, v223
	v_and_b32_e32 v79, 0xffff0000, v223
	v_pk_add_f32 v[158:159], v[158:159], v[78:79]
	s_cmp_lt_u32 s12, 3
	s_cbranch_scc1 .Lfin_accd1
	v_lshlrev_b32_e32 v78, 16, v224
	v_and_b32_e32 v79, 0xffff0000, v224
	v_pk_add_f32 v[144:145], v[144:145], v[78:79]
	v_lshlrev_b32_e32 v78, 16, v225
	v_and_b32_e32 v79, 0xffff0000, v225
	v_pk_add_f32 v[146:147], v[146:147], v[78:79]
	v_lshlrev_b32_e32 v78, 16, v226
	v_and_b32_e32 v79, 0xffff0000, v226
	v_pk_add_f32 v[148:149], v[148:149], v[78:79]
	v_lshlrev_b32_e32 v78, 16, v227
	v_and_b32_e32 v79, 0xffff0000, v227
	v_pk_add_f32 v[150:151], v[150:151], v[78:79]
	v_lshlrev_b32_e32 v78, 16, v228
	v_and_b32_e32 v79, 0xffff0000, v228
	v_pk_add_f32 v[152:153], v[152:153], v[78:79]
	v_lshlrev_b32_e32 v78, 16, v229
	v_and_b32_e32 v79, 0xffff0000, v229
	v_pk_add_f32 v[154:155], v[154:155], v[78:79]
	v_lshlrev_b32_e32 v78, 16, v230
	v_and_b32_e32 v79, 0xffff0000, v230
	v_pk_add_f32 v[156:157], v[156:157], v[78:79]
	v_lshlrev_b32_e32 v78, 16, v231
	v_and_b32_e32 v79, 0xffff0000, v231
	v_pk_add_f32 v[158:159], v[158:159], v[78:79]
	s_cmp_lt_u32 s12, 4
	s_cbranch_scc1 .Lfin_accd1
	v_lshlrev_b32_e32 v78, 16, v232
	v_and_b32_e32 v79, 0xffff0000, v232
	v_pk_add_f32 v[144:145], v[144:145], v[78:79]
	v_lshlrev_b32_e32 v78, 16, v233
	v_and_b32_e32 v79, 0xffff0000, v233
	v_pk_add_f32 v[146:147], v[146:147], v[78:79]
	v_lshlrev_b32_e32 v78, 16, v234
	v_and_b32_e32 v79, 0xffff0000, v234
	v_pk_add_f32 v[148:149], v[148:149], v[78:79]
	v_lshlrev_b32_e32 v78, 16, v235
	v_and_b32_e32 v79, 0xffff0000, v235
	v_pk_add_f32 v[150:151], v[150:151], v[78:79]
	v_lshlrev_b32_e32 v78, 16, v236
	v_and_b32_e32 v79, 0xffff0000, v236
	v_pk_add_f32 v[152:153], v[152:153], v[78:79]
	v_lshlrev_b32_e32 v78, 16, v237
	v_and_b32_e32 v79, 0xffff0000, v237
	v_pk_add_f32 v[154:155], v[154:155], v[78:79]
	v_lshlrev_b32_e32 v78, 16, v238
	v_and_b32_e32 v79, 0xffff0000, v238
	v_pk_add_f32 v[156:157], v[156:157], v[78:79]
	v_lshlrev_b32_e32 v78, 16, v239
	v_and_b32_e32 v79, 0xffff0000, v239
	v_pk_add_f32 v[158:159], v[158:159], v[78:79]
	s_cmp_lt_u32 s12, 5
	s_cbranch_scc1 .Lfin_accd1
	v_lshlrev_b32_e32 v78, 16, v240
	v_and_b32_e32 v79, 0xffff0000, v240
	v_pk_add_f32 v[144:145], v[144:145], v[78:79]
	v_lshlrev_b32_e32 v78, 16, v241
	v_and_b32_e32 v79, 0xffff0000, v241
	v_pk_add_f32 v[146:147], v[146:147], v[78:79]
	v_lshlrev_b32_e32 v78, 16, v242
	v_and_b32_e32 v79, 0xffff0000, v242
	v_pk_add_f32 v[148:149], v[148:149], v[78:79]
	v_lshlrev_b32_e32 v78, 16, v243
	v_and_b32_e32 v79, 0xffff0000, v243
	v_pk_add_f32 v[150:151], v[150:151], v[78:79]
	v_lshlrev_b32_e32 v78, 16, v244
	v_and_b32_e32 v79, 0xffff0000, v244
	v_pk_add_f32 v[152:153], v[152:153], v[78:79]
	v_lshlrev_b32_e32 v78, 16, v245
	v_and_b32_e32 v79, 0xffff0000, v245
	v_pk_add_f32 v[154:155], v[154:155], v[78:79]
	v_lshlrev_b32_e32 v78, 16, v246
	v_and_b32_e32 v79, 0xffff0000, v246
	v_pk_add_f32 v[156:157], v[156:157], v[78:79]
	v_lshlrev_b32_e32 v78, 16, v247
	v_and_b32_e32 v79, 0xffff0000, v247
	v_pk_add_f32 v[158:159], v[158:159], v[78:79]
	s_cmp_lt_u32 s12, 6
	s_cbranch_scc1 .Lfin_accd1
	v_lshlrev_b32_e32 v78, 16, v248
	v_and_b32_e32 v79, 0xffff0000, v248
	v_pk_add_f32 v[144:145], v[144:145], v[78:79]
	v_lshlrev_b32_e32 v78, 16, v249
	v_and_b32_e32 v79, 0xffff0000, v249
	v_pk_add_f32 v[146:147], v[146:147], v[78:79]
	v_lshlrev_b32_e32 v78, 16, v250
	v_and_b32_e32 v79, 0xffff0000, v250
	v_pk_add_f32 v[148:149], v[148:149], v[78:79]
	v_lshlrev_b32_e32 v78, 16, v251
	v_and_b32_e32 v79, 0xffff0000, v251
	v_pk_add_f32 v[150:151], v[150:151], v[78:79]
	v_lshlrev_b32_e32 v78, 16, v252
	v_and_b32_e32 v79, 0xffff0000, v252
	v_pk_add_f32 v[152:153], v[152:153], v[78:79]
	v_lshlrev_b32_e32 v78, 16, v253
	v_and_b32_e32 v79, 0xffff0000, v253
	v_pk_add_f32 v[154:155], v[154:155], v[78:79]
	v_lshlrev_b32_e32 v78, 16, v254
	v_and_b32_e32 v79, 0xffff0000, v254
	v_pk_add_f32 v[156:157], v[156:157], v[78:79]
	v_lshlrev_b32_e32 v78, 16, v255
	v_and_b32_e32 v79, 0xffff0000, v255
	v_pk_add_f32 v[158:159], v[158:159], v[78:79]
.Lfin_ovf1:
	s_cmp_eq_u32 s10, 0
	s_cbranch_scc1 .Lfin_accd1
	s_ff1_i32_b32 s26, s10
	s_bitset0_b32 s10, s26
	s_add_i32 s27, s26, 16
	v_readlane_b32 s30, v76, s27
	s_lshl_b32 s26, s26, 11
	s_add_i32 s26, s26, s22
	s_add_i32 s26, s26, s30
	s_lshl_b32 s26, s26, 11
	s_add_u32 s24, s14, s26
	s_addc_u32 s25, s15, 0
	global_load_dwordx4 v[208:211], v1, s[24:25]
	global_load_dwordx4 v[212:215], v1, s[24:25] offset:1024
	s_waitcnt vmcnt(0)
	v_lshlrev_b32_e32 v78, 16, v208
	v_and_b32_e32 v79, 0xffff0000, v208
	v_pk_add_f32 v[144:145], v[144:145], v[78:79]
	v_lshlrev_b32_e32 v78, 16, v209
	v_and_b32_e32 v79, 0xffff0000, v209
	v_pk_add_f32 v[146:147], v[146:147], v[78:79]
	v_lshlrev_b32_e32 v78, 16, v210
	v_and_b32_e32 v79, 0xffff0000, v210
	v_pk_add_f32 v[148:149], v[148:149], v[78:79]
	v_lshlrev_b32_e32 v78, 16, v211
	v_and_b32_e32 v79, 0xffff0000, v211
	v_pk_add_f32 v[150:151], v[150:151], v[78:79]
	v_lshlrev_b32_e32 v78, 16, v212
	v_and_b32_e32 v79, 0xffff0000, v212
	v_pk_add_f32 v[152:153], v[152:153], v[78:79]
	v_lshlrev_b32_e32 v78, 16, v213
	v_and_b32_e32 v79, 0xffff0000, v213
	v_pk_add_f32 v[154:155], v[154:155], v[78:79]
	v_lshlrev_b32_e32 v78, 16, v214
	v_and_b32_e32 v79, 0xffff0000, v214
	v_pk_add_f32 v[156:157], v[156:157], v[78:79]
	v_lshlrev_b32_e32 v78, 16, v215
	v_and_b32_e32 v79, 0xffff0000, v215
	v_pk_add_f32 v[158:159], v[158:159], v[78:79]
	s_branch .Lfin_ovf1
.Lfin_accd1:
	v_pk_fma_f32 v[96:97], v[128:129], v[60:61], v[96:97]
	v_pk_fma_f32 v[98:99], v[130:131], v[62:63], v[98:99]
	v_pk_fma_f32 v[100:101], v[132:133], v[64:65], v[100:101]
	v_pk_fma_f32 v[102:103], v[134:135], v[66:67], v[102:103]
	v_pk_fma_f32 v[104:105], v[136:137], v[68:69], v[104:105]
	v_pk_fma_f32 v[106:107], v[138:139], v[70:71], v[106:107]
	v_pk_fma_f32 v[108:109], v[140:141], v[72:73], v[108:109]
	v_pk_fma_f32 v[110:111], v[142:143], v[74:75], v[110:111]
	v_pk_fma_f32 v[112:113], v[144:145], v[60:61], v[112:113]
	v_pk_fma_f32 v[114:115], v[146:147], v[62:63], v[114:115]
	v_pk_fma_f32 v[116:117], v[148:149], v[64:65], v[116:117]
	v_pk_fma_f32 v[118:119], v[150:151], v[66:67], v[118:119]
	v_pk_fma_f32 v[120:121], v[152:153], v[68:69], v[120:121]
	v_pk_fma_f32 v[122:123], v[154:155], v[70:71], v[122:123]
	v_pk_fma_f32 v[124:125], v[156:157], v[72:73], v[124:125]
	v_pk_fma_f32 v[126:127], v[158:159], v[74:75], v[126:127]
	v_mul_f32_e32 v160, v96, v96
	v_mul_f32_e32 v162, v112, v112
	v_fmac_f32_e32 v160, v97, v97
	v_fmac_f32_e32 v162, v113, v113
	v_fmac_f32_e32 v160, v98, v98
	v_fmac_f32_e32 v162, v114, v114
	v_fmac_f32_e32 v160, v99, v99
	v_fmac_f32_e32 v162, v115, v115
	v_fmac_f32_e32 v160, v100, v100
	v_fmac_f32_e32 v162, v116, v116
	v_fmac_f32_e32 v160, v101, v101
	v_fmac_f32_e32 v162, v117, v117
	v_fmac_f32_e32 v160, v102, v102
	v_fmac_f32_e32 v162, v118, v118
	v_fmac_f32_e32 v160, v103, v103
	v_fmac_f32_e32 v162, v119, v119
	v_fmac_f32_e32 v160, v104, v104
	v_fmac_f32_e32 v162, v120, v120
	v_fmac_f32_e32 v160, v105, v105
	v_fmac_f32_e32 v162, v121, v121
	v_fmac_f32_e32 v160, v106, v106
	v_fmac_f32_e32 v162, v122, v122
	v_fmac_f32_e32 v160, v107, v107
	v_fmac_f32_e32 v162, v123, v123
	v_fmac_f32_e32 v160, v108, v108
	v_fmac_f32_e32 v162, v124, v124
	v_fmac_f32_e32 v160, v109, v109
	v_fmac_f32_e32 v162, v125, v125
	v_fmac_f32_e32 v160, v110, v110
	v_fmac_f32_e32 v162, v126, v126
	v_fmac_f32_e32 v160, v111, v111
	v_fmac_f32_e32 v162, v127, v127
	ds_bpermute_b32 v164, v4, v160
	ds_bpermute_b32 v165, v4, v162
	s_waitcnt lgkmcnt(1)
	v_add_f32_e32 v160, v160, v164
	s_waitcnt lgkmcnt(0)
	v_add_f32_e32 v162, v162, v165
	ds_bpermute_b32 v164, v5, v160
	ds_bpermute_b32 v165, v5, v162
	s_waitcnt lgkmcnt(1)
	v_add_f32_e32 v160, v160, v164
	s_waitcnt lgkmcnt(0)
	v_add_f32_e32 v162, v162, v165
	ds_bpermute_b32 v164, v6, v160
	ds_bpermute_b32 v165, v6, v162
	s_waitcnt lgkmcnt(1)
	v_add_f32_e32 v160, v160, v164
	s_waitcnt lgkmcnt(0)
	v_add_f32_e32 v162, v162, v165
	ds_bpermute_b32 v164, v7, v160
	ds_bpermute_b32 v165, v7, v162
	s_waitcnt lgkmcnt(1)
	v_add_f32_e32 v160, v160, v164
	s_waitcnt lgkmcnt(0)
	v_add_f32_e32 v162, v162, v165
	ds_bpermute_b32 v164, v8, v160
	ds_bpermute_b32 v165, v8, v162
	s_waitcnt lgkmcnt(1)
	v_add_f32_e32 v160, v160, v164
	s_waitcnt lgkmcnt(0)
	v_add_f32_e32 v162, v162, v165
	ds_bpermute_b32 v164, v9, v160
	ds_bpermute_b32 v165, v9, v162
	s_waitcnt lgkmcnt(1)
	v_add_f32_e32 v160, v160, v164
	s_waitcnt lgkmcnt(0)
	v_add_f32_e32 v162, v162, v165
	v_fma_f32 v160, v160, s23, v10
	v_fma_f32 v162, v162, s23, v10
	v_rsq_f32_e32 v160, v160
	v_rsq_f32_e32 v162, v162
	s_lshl_b32 s26, s6, 12
	s_add_u32 s28, s2, s26
	s_addc_u32 s29, s3, 0
	s_add_u32 s30, s28, 0x1000
	s_addc_u32 s31, s29, 0
	v_pk_mul_f32 v[96:97], v[96:97], v[160:161] op_sel_hi:[1,0]
	v_pk_mul_f32 v[98:99], v[98:99], v[160:161] op_sel_hi:[1,0]
	v_pk_mul_f32 v[100:101], v[100:101], v[160:161] op_sel_hi:[1,0]
	v_pk_mul_f32 v[102:103], v[102:103], v[160:161] op_sel_hi:[1,0]
	v_pk_mul_f32 v[104:105], v[104:105], v[160:161] op_sel_hi:[1,0]
	v_pk_mul_f32 v[106:107], v[106:107], v[160:161] op_sel_hi:[1,0]
	v_pk_mul_f32 v[108:109], v[108:109], v[160:161] op_sel_hi:[1,0]
	v_pk_mul_f32 v[110:111], v[110:111], v[160:161] op_sel_hi:[1,0]
	v_pk_mul_f32 v[96:97], v[96:97], v[12:13]
	v_pk_mul_f32 v[98:99], v[98:99], v[14:15]
	v_pk_mul_f32 v[100:101], v[100:101], v[16:17]
	v_pk_mul_f32 v[102:103], v[102:103], v[18:19]
	v_pk_mul_f32 v[104:105], v[104:105], v[20:21]
	v_pk_mul_f32 v[106:107], v[106:107], v[22:23]
	v_pk_mul_f32 v[108:109], v[108:109], v[24:25]
	v_pk_mul_f32 v[110:111], v[110:111], v[26:27]
	global_store_dwordx4 v2, v[96:99], s[28:29]
	global_store_dwordx4 v2, v[100:103], s[28:29] offset:16
	global_store_dwordx4 v2, v[104:107], s[28:29] offset:2048
	global_store_dwordx4 v2, v[108:111], s[28:29] offset:2064
	v_pk_mul_f32 v[112:113], v[112:113], v[162:163] op_sel_hi:[1,0]
	v_pk_mul_f32 v[114:115], v[114:115], v[162:163] op_sel_hi:[1,0]
	v_pk_mul_f32 v[116:117], v[116:117], v[162:163] op_sel_hi:[1,0]
	v_pk_mul_f32 v[118:119], v[118:119], v[162:163] op_sel_hi:[1,0]
	v_pk_mul_f32 v[120:121], v[120:121], v[162:163] op_sel_hi:[1,0]
	v_pk_mul_f32 v[122:123], v[122:123], v[162:163] op_sel_hi:[1,0]
	v_pk_mul_f32 v[124:125], v[124:125], v[162:163] op_sel_hi:[1,0]
	v_pk_mul_f32 v[126:127], v[126:127], v[162:163] op_sel_hi:[1,0]
	v_pk_mul_f32 v[112:113], v[112:113], v[12:13]
	v_pk_mul_f32 v[114:115], v[114:115], v[14:15]
	v_pk_mul_f32 v[116:117], v[116:117], v[16:17]
	v_pk_mul_f32 v[118:119], v[118:119], v[18:19]
	v_pk_mul_f32 v[120:121], v[120:121], v[20:21]
	v_pk_mul_f32 v[122:123], v[122:123], v[22:23]
	v_pk_mul_f32 v[124:125], v[124:125], v[24:25]
	v_pk_mul_f32 v[126:127], v[126:127], v[26:27]
	global_store_dwordx4 v2, v[112:115], s[30:31]
	global_store_dwordx4 v2, v[116:119], s[30:31] offset:16
	global_store_dwordx4 v2, v[120:123], s[30:31] offset:2048
	global_store_dwordx4 v2, v[124:127], s[30:31] offset:2064
	s_mov_b32 s6, s8
	s_cmp_lt_u32 s6, 0x4000
	s_cbranch_scc1 .Lfin_loop
